# v16 + last quarter (3 items per wave) of layer-0 W2 conversion deferred to idle WGs of P1
# speedup vs baseline: 1.0056x; 1.0056x over previous
; DI void phase_prologue(const Ctx& C) {
;     const int gw = C.gw, ngw = C.ngw, lane = C.lane;
;     for (int it = gw; it < LAYER_ITEMS; it += ngw) convert_layer_item(C, 0, it, lane);
.LBB0_5:
	s_or_b64 exec, exec, s[4:5]
	s_lshr_b32 s13, s12, 6
	s_lshl_b32 s3, s2, 3
	s_add_i32 s94, s13, s3
	s_lshl_b32 s82, s33, 3
	s_cmp_lt_i32 s92, 1
	s_cselect_b64 s[4:5], -1, 0
	s_cmp_gt_i32 s93, 0
	s_cselect_b64 s[6:7], -1, 0
	s_and_b64 s[4:5], s[4:5], s[6:7]
	s_andn2_b64 vcc, exec, s[4:5]
	s_mov_b64 s[4:5], s[42:43]
	v_writelane_b32 v251, s4, 2
	s_nop 1
	v_writelane_b32 v251, s5, 3
	s_cbranch_vccnz .LBB0_163
s_mov_b32 s100, 0x23ff
s_mov_b32 s101, 0

; #define PH_END   if (p + 1 < hi) xcd_barrier(bar, C.tid); else __syncthreads(); } ++p;
; DI void phase_prologue(const Ctx& C) {
;     ...
;     for (int it = gw; it < LAYER_ITEMS; it += ngw) convert_layer_item(C, 0, it, lane);
; __global__ void __launch_bounds__(NTHREADS, 2) mk_fwd(Args args) {
;     ...
;     PH_BEGIN
;         pg8::MultiOrder S{(const char*)WSP(unsigned char, WS_MEMB), (const char*)WSP(unsigned char, WS_WKV), 0, 0, 0, (size_t)4096 * D, 0, 0, 0, 0, 0, 2, 16, NL, D / 2, D / 2, XCD_G(128), XCD_C(128)};
;         pg8::EpiStore<2, false, true> E{WSP(bf16_t, WS_KVB), (size_t)MT * 4096, 0, 0, 0, 4096, WSP(float, WS_RMEM), 0, 1.f / W8S};
;         pg8::gemm_phase<pg8::EpiStore<2, false, true>, pg8::MultiOrder, true, false, true>(C.lds, C.tid, D / 2, D / 2, D / 2, S, E);
;     PH_END
.Lp1_detour:
	s_add_i32 s94, s94, 0x2000
	s_movk_i32 s82, 0x400
	s_mov_b32 s100, 0x2fff
	s_mov_b32 s101, 1
	s_branch .Lp0_conv_entry
.Lp1_conv_ret:
	s_sub_i32 s94, s94, 0x2000
	s_lshl_b32 s82, s33, 3
	s_mov_b32 s101, 0
